# c_proj_w f32->f16 conversion moved from cvt3 into attention pass-0 tile loop (pointer via ws+96MiB); sc1 stores
# speedup vs baseline: 1.0127x; 1.0028x over previous
.LBB0_4:
	s_cmp_lg_u32 s3, 0
	s_cbranch_scc1 .LBB0_16
	s_load_dwordx2 s[4:5], s[0:1], 0x30
	s_load_dwordx2 s[6:7], s[0:1], 0x8
	s_waitcnt lgkmcnt(0)
	s_add_u32 s6, s6, 0x6000000
	s_addc_u32 s7, s7, 0
	v_mov_b32_e32 v2, s4
	v_mov_b32_e32 v3, s5
	v_mov_b32_e32 v4, 0
	global_store_dwordx2 v4, v[2:3], s[6:7]
	s_branch .LBB0_16

.LBB3_2:
	s_and_b32 s96, s8, 3
	s_lshl_b32 s9, s4, 14
	s_cmp_lg_u32 0, -1
	s_cselect_b32 s10, 0, 0
	s_lshl_b64 s[0:1], s[0:1], 1
	s_add_u32 s72, s64, s0
	s_addc_u32 s11, s65, s1
	s_add_i32 s8, s9, 0
	s_bfe_u32 s33, s2, 0x40003
	s_add_i32 s12, s8, 0x10000
	s_add_u32 s64, s60, s0
	s_addc_u32 s65, s61, s1
	s_add_u32 s100, s60, 0x3000000
	s_addc_u32 s101, s61, 0
	s_load_dwordx2 s[62:63], s[100:101], 0x0
	s_xor_b32 s99, s33, 31
	v_and_b32_e32 v207, 31, v0
	s_lshl_b32 s8, s99, 7
	v_lshlrev_b32_e32 v4, 4, v0
	v_bfe_u32 v160, v0, 5, 1
	s_lshl_b32 s79, s96, 5
	v_or_b32_e32 v11, s8, v207
	v_lshlrev_b32_e32 v184, 4, v160
	v_mov_b32_e32 v185, 0
	v_lshlrev_b32_e32 v5, 8, v207
	v_and_b32_e32 v6, 0x70, v4
	v_or_b32_e32 v161, s79, v11
	v_lshl_add_u64 v[2:3], s[64:65], 0, v[184:185]
	v_bitop3_b32 v7, v184, v5, v6 bitop3:0xde
	v_or_b32_e32 v8, 32, v184
	v_or_b32_e32 v9, 64, v184
	v_or_b32_e32 v10, 0x60, v184
	v_lshlrev_b32_e32 v184, 8, v161
	v_lshl_add_u64 v[2:3], v[2:3], 0, v[184:185]
	global_load_dwordx4 v[156:159], v[2:3], off
	global_load_dwordx4 v[152:155], v[2:3], off offset:32
	global_load_dwordx4 v[148:151], v[2:3], off offset:64
	global_load_dwordx4 v[144:147], v[2:3], off offset:96
	global_load_dwordx4 v[140:143], v[2:3], off offset:128
	global_load_dwordx4 v[136:139], v[2:3], off offset:160
	global_load_dwordx4 v[132:135], v[2:3], off offset:192
	global_load_dwordx4 v[128:131], v[2:3], off offset:224
	v_and_b32_e32 v2, 63, v0
	v_lshlrev_b32_e32 v2, 3, v2
	v_and_b32_e32 v4, 0xc0, v4
	v_lshlrev_b32_e32 v11, 1, v0
	v_and_b32_e32 v3, 24, v2
	v_and_b32_e32 v11, 32, v11
	v_add_u32_e32 v4, s10, v4
	v_add3_u32 v3, v4, v11, v3
	v_and_b32_e32 v4, 16, v1
	v_lshlrev_b32_e32 v1, 3, v1
	v_lshrrev_b32_e32 v11, 5, v0
	v_and_b32_e32 v1, 8, v1
	v_bfe_u32 v12, v0, 2, 2
	v_and_or_b32 v4, v11, 4, v4
	v_or3_b32 v1, v4, v12, v1
	v_and_b32_e32 v4, 0x60, v0
	v_lshlrev_b32_e32 v0, 3, v0
	v_and_or_b32 v0, v0, 24, v4
	v_lshlrev_b32_e32 v0, 1, v0
	v_lshl_or_b32 v186, v1, 8, v0
	v_bitop3_b32 v0, v8, v5, v6 bitop3:0xde
	v_add_u32_e32 v189, s12, v0
	v_bitop3_b32 v0, v9, v5, v6 bitop3:0xde
	s_waitcnt vmcnt(0) lgkmcnt(0)
	s_barrier
	s_lshl_b32 s101, s2, 16
	s_add_u32 s62, s62, s101
	s_addc_u32 s63, s63, 0
	s_lshl_b32 s101, s2, 15
	s_sub_u32 s60, s60, 0x800000
	s_subb_u32 s61, s61, 0
	s_add_u32 s60, s60, s101
	s_addc_u32 s61, s61, 0
	s_mov_b32 s100, 0
	v_and_b32_e32 v2, 0x100, v2
	v_add_u32_e32 v188, s12, v0
	v_bitop3_b32 v0, v10, v5, v6 bitop3:0xde
	v_add3_u32 v184, v3, v2, s9
	s_and_b32 s73, s11, 0xffff
	s_mov_b32 s74, s70
	s_mov_b32 s75, s71
	v_add_u32_e32 v190, s12, v7
	v_add_u32_e32 v187, s12, v0
	s_add_i32 s91, s3, 0x18000
	s_add_i32 s92, s3, 0x1a000
	s_add_i32 s93, s3, 0x1c000
	s_mov_b32 s0, 0x1e000
	s_add_i32 s94, s3, 0x1e000
	s_add_i32 s82, s3, 0x2000
	s_add_i32 s81, s3, 0x4000
	s_add_i32 s80, s3, 0x6000
	s_add_i32 s90, s3, 0x8000
	s_add_i32 s89, s3, 0xa000
	s_add_i32 s88, s3, 0xc000
	s_add_i32 s87, s3, 0xe000
	s_mov_b32 s1, 0x8000
	s_mov_b32 s9, 0xa000
	s_mov_b32 s10, 0xc000
	s_mov_b32 s11, 0xe000
	ds_read_b128 v[16:19], v190
	ds_read_b128 v[20:23], v190 offset:8192
	s_mov_b32 m0, s91
	s_waitcnt vmcnt(7) lgkmcnt(1)
	v_mfma_f32_32x32x16_f16 v[0:15], v[16:19], v[156:159], -0.5
	buffer_load_dwordx4 v191, s[68:71], s1 offen lds
	ds_read_b128 v[24:27], v189
	ds_read_b128 v[16:19], v189 offset:8192
	s_mov_b32 m0, s92
	s_waitcnt lgkmcnt(2)
	v_mfma_f32_32x32x16_f16 v[96:111], v[20:23], v[156:159], -0.5
	s_waitcnt vmcnt(7) lgkmcnt(1)
	v_mfma_f32_32x32x16_f16 v[0:15], v[24:27], v[152:155], v[0:15]
	buffer_load_dwordx4 v191, s[68:71], s9 offen lds
	s_mov_b32 m0, s93
	s_waitcnt lgkmcnt(0)
	v_mfma_f32_32x32x16_f16 v[96:111], v[16:19], v[152:155], v[96:111]
	ds_read_b128 v[16:19], v188
	s_waitcnt vmcnt(7) lgkmcnt(0)
	v_mfma_f32_32x32x16_f16 v[0:15], v[16:19], v[148:151], v[0:15]
	ds_read_b128 v[16:19], v188 offset:8192
	buffer_load_dwordx4 v191, s[68:71], s10 offen lds
	s_mov_b32 m0, s94
	s_waitcnt lgkmcnt(0)
	v_mfma_f32_32x32x16_f16 v[96:111], v[16:19], v[148:151], v[96:111]
	ds_read_b128 v[16:19], v187
	s_waitcnt vmcnt(7) lgkmcnt(0)
	v_mfma_f32_32x32x16_f16 v[0:15], v[16:19], v[144:147], v[0:15]
	ds_read_b128 v[16:19], v187 offset:8192
	buffer_load_dwordx4 v191, s[68:71], s11 offen lds
	s_mov_b32 m0, s3
	s_waitcnt lgkmcnt(0)
	v_mfma_f32_32x32x16_f16 v[96:111], v[16:19], v[144:147], v[96:111]
	ds_read_b128 v[16:19], v190 offset:128
	s_waitcnt vmcnt(7) lgkmcnt(0)
	v_mfma_f32_32x32x16_f16 v[0:15], v[16:19], v[140:143], v[0:15]
	ds_read_b128 v[16:19], v190 offset:8320
	buffer_load_dwordx4 v186, s[72:75], 0 offen lds
	s_mov_b32 m0, s82
	s_waitcnt lgkmcnt(0)
	v_mfma_f32_32x32x16_f16 v[96:111], v[16:19], v[140:143], v[96:111]
	ds_read_b128 v[16:19], v189 offset:128
	s_waitcnt vmcnt(7) lgkmcnt(0)
	v_mfma_f32_32x32x16_f16 v[0:15], v[16:19], v[136:139], v[0:15]
	ds_read_b128 v[16:19], v189 offset:8320
	buffer_load_dwordx4 v186, s[72:75], s7 offen lds
	s_mov_b32 m0, s81
	s_waitcnt lgkmcnt(0)
	v_mfma_f32_32x32x16_f16 v[96:111], v[16:19], v[136:139], v[96:111]
	ds_read_b128 v[16:19], v188 offset:128
	s_waitcnt vmcnt(7) lgkmcnt(0)
	v_mfma_f32_32x32x16_f16 v[0:15], v[16:19], v[132:135], v[0:15]
	ds_read_b128 v[16:19], v188 offset:8320
	buffer_load_dwordx4 v186, s[72:75], s6 offen lds
	s_mov_b32 m0, s80
	s_waitcnt lgkmcnt(0)
	v_mfma_f32_32x32x16_f16 v[96:111], v[16:19], v[132:135], v[96:111]
	ds_read_b128 v[16:19], v187 offset:128
	ds_read_b128 v[20:23], v187 offset:8320
	buffer_load_dwordx4 v186, s[72:75], s5 offen lds
	s_waitcnt vmcnt(0) lgkmcnt(0)
	s_barrier
	s_waitcnt vmcnt(8) lgkmcnt(0)
	v_mfma_f32_32x32x16_f16 v[96:111], v[20:23], v[128:131], v[96:111]
	v_mfma_f32_32x32x16_f16 v[0:15], v[16:19], v[128:131], v[0:15]
	s_nop 11
	v_exp_f32_e32 v210, v0
	v_exp_f32_e32 v211, v1
	v_exp_f32_e32 v212, v2
	v_exp_f32_e32 v213, v3
	v_exp_f32_e32 v214, v4
	v_exp_f32_e32 v215, v5
	v_exp_f32_e32 v216, v6
	v_exp_f32_e32 v217, v7
	v_exp_f32_e32 v218, v8
	v_exp_f32_e32 v219, v9
	v_exp_f32_e32 v220, v10
	v_exp_f32_e32 v221, v11
	v_exp_f32_e32 v222, v12
	v_exp_f32_e32 v223, v13
	v_exp_f32_e32 v224, v14
	v_exp_f32_e32 v225, v15
	v_mov_b32_e32 v16, v185
	v_mov_b32_e32 v17, v185
	v_mov_b32_e32 v18, v185
	v_mov_b32_e32 v19, v185
	v_mov_b32_e32 v20, v185
	v_mov_b32_e32 v21, v185
	v_mov_b32_e32 v22, v185
	v_mov_b32_e32 v23, v185
	v_mov_b32_e32 v24, v185
	v_mov_b32_e32 v25, v185
	v_mov_b32_e32 v26, v185
	v_mov_b32_e32 v27, v185
	v_mov_b32_e32 v28, v185
	v_mov_b32_e32 v29, v185
	v_mov_b32_e32 v30, v185
	v_mov_b32_e32 v31, v185
	v_mov_b32_e32 v32, v185
	v_mov_b32_e32 v33, v185
	v_mov_b32_e32 v34, v185
	v_mov_b32_e32 v35, v185
	v_mov_b32_e32 v36, v185
	v_mov_b32_e32 v37, v185
	v_mov_b32_e32 v38, v185
	v_mov_b32_e32 v39, v185
	v_mov_b32_e32 v40, v185
	v_mov_b32_e32 v41, v185
	v_mov_b32_e32 v42, v185
	v_mov_b32_e32 v43, v185
	v_mov_b32_e32 v44, v185
	v_mov_b32_e32 v45, v185
	v_mov_b32_e32 v46, v185
	v_mov_b32_e32 v47, v185
	v_mov_b32_e32 v48, v185
	v_mov_b32_e32 v49, v185
	v_mov_b32_e32 v50, v185
	v_mov_b32_e32 v51, v185
	v_mov_b32_e32 v52, v185
	v_mov_b32_e32 v53, v185
	v_mov_b32_e32 v54, v185
	v_mov_b32_e32 v55, v185
	v_mov_b32_e32 v56, v185
	v_mov_b32_e32 v57, v185
	v_mov_b32_e32 v58, v185
	v_mov_b32_e32 v59, v185
	v_mov_b32_e32 v60, v185
	v_mov_b32_e32 v61, v185
	v_mov_b32_e32 v62, v185
	v_mov_b32_e32 v63, v185
	v_mov_b32_e32 v64, v185
	v_mov_b32_e32 v65, v185
	v_mov_b32_e32 v66, v185
	v_mov_b32_e32 v67, v185
	v_mov_b32_e32 v68, v185
	v_mov_b32_e32 v69, v185
	v_mov_b32_e32 v70, v185
	v_mov_b32_e32 v71, v185
	v_mov_b32_e32 v72, v185
	v_mov_b32_e32 v73, v185
	v_mov_b32_e32 v74, v185
	v_mov_b32_e32 v75, v185
	v_mov_b32_e32 v76, v185
	v_mov_b32_e32 v77, v185
	v_mov_b32_e32 v78, v185
	v_mov_b32_e32 v79, v185
.LBB3_3:
	s_cmp_gt_u32 s100, 8
	s_cbranch_scc1 .Lcw_a_done
	s_cmp_eq_u32 s100, 0
	s_cbranch_scc1 .Lcw_a_load
	v_cvt_pk_f16_f32 v252, v252, v253
	v_cvt_pk_f16_f32 v253, v254, v255
	v_lshrrev_b32_e32 v254, 1, v191
	global_store_dwordx2 v254, v[252:253], s[60:61]
	s_add_u32 s60, s60, 0x1000
	s_addc_u32 s61, s61, 0
	s_cmp_eq_u32 s100, 8
	s_cbranch_scc1 .Lcw_a_inc
.Lcw_a_load:
	global_load_dwordx4 v[252:255], v191, s[62:63]
	s_add_u32 s62, s62, 0x2000
	s_addc_u32 s63, s63, 0
.Lcw_a_inc:
	s_add_i32 s100, s100, 1
.Lcw_a_done:
	s_mov_b32 s1, s97
	s_mov_b32 m0, s86
	s_add_i32 s5, s0, 0xffff2000
	ds_read_b128 v[0:3], v190 offset:32768
	ds_read_b128 v[112:115], v190 offset:40960
	buffer_load_dwordx4 v191, s[68:71], s5 offen lds
	ds_read_b128 v[4:7], v189 offset:32768
	ds_read_b128 v[116:119], v189 offset:40960
	s_add_i32 s6, s0, 0xffff4000
	s_mov_b32 m0, s85
	s_waitcnt lgkmcnt(3)
	v_mfma_f32_32x32x16_f16 v[80:95], v[0:3], v[156:159], -0.5
	s_add_i32 s7, s0, 0xffff6000
	buffer_load_dwordx4 v191, s[68:71], s6 offen lds
	s_waitcnt lgkmcnt(1)
	v_mfma_f32_32x32x16_f16 v[80:95], v[4:7], v[152:155], v[80:95]
	v_mfma_f32_32x32x16_f16 v[0:15], v[112:115], v[156:159], -0.5
	ds_read_b128 v[112:115], v188 offset:32768
	s_mov_b32 m0, s84
	s_add_i32 s9, s0, 0xffff8000
	s_add_i32 s10, s0, 0xfffea000
	v_exp_f32_e32 v182, v100
	v_exp_f32_e32 v183, v101
	s_waitcnt lgkmcnt(1)
	v_mfma_f32_32x32x16_f16 v[0:15], v[116:119], v[152:155], v[0:15]
	ds_read_b128 v[116:119], v188 offset:40960
	buffer_load_dwordx4 v191, s[68:71], s7 offen lds
	s_mov_b32 m0, s83
	v_exp_f32_e32 v192, v106
	v_exp_f32_e32 v193, v107
	v_exp_f32_e32 v194, v108
	v_exp_f32_e32 v111, v111
	s_waitcnt lgkmcnt(1)
	v_mfma_f32_32x32x16_f16 v[80:95], v[112:115], v[148:151], v[80:95]
	ds_read_b128 v[112:115], v187 offset:32768
	ds_read_b128 v[120:123], v187 offset:40960
	buffer_load_dwordx4 v191, s[68:71], s9 offen lds
	s_mov_b32 m0, s90
	ds_read_b128 v[124:127], v190 offset:32896
	ds_read_b128 v[162:165], v190 offset:41088
	buffer_load_dwordx4 v186, s[72:75], s10 offen lds
	s_add_i32 s10, s0, 0xfffec000
	s_mov_b32 m0, s89
	s_waitcnt lgkmcnt(4)
	v_mfma_f32_32x32x16_f16 v[0:15], v[116:119], v[148:151], v[0:15]
	ds_read_b128 v[116:119], v189 offset:32896
	ds_read_b128 v[166:169], v189 offset:41088
	buffer_load_dwordx4 v186, s[72:75], s10 offen lds
	s_add_i32 s10, s0, 0xfffee000
	s_mov_b32 m0, s88
	v_cvt_pk_f16_f32 v100, v218, v219
	v_cvt_pk_f16_f32 v101, v220, v221
	v_cvt_pk_f16_f32 v106, v182, v183
	s_waitcnt lgkmcnt(5)
	v_mfma_f32_32x32x16_f16 v[80:95], v[112:115], v[144:147], v[80:95]
	ds_read_b128 v[112:115], v188 offset:32896
	ds_read_b128 v[170:173], v188 offset:41088
	buffer_load_dwordx4 v186, s[72:75], s10 offen lds
	s_add_i32 s10, s0, 0xffff0000
	s_mov_b32 m0, s87
	ds_read_b128 v[174:177], v187 offset:32896
	ds_read_b128 v[178:181], v187 offset:41088
	buffer_load_dwordx4 v186, s[72:75], s10 offen lds
	s_waitcnt lgkmcnt(8)
	v_mfma_f32_32x32x16_f16 v[0:15], v[120:123], v[144:147], v[0:15]
	v_exp_f32_e32 v120, v96
	v_add_f32_e32 v96, 0, v210
	v_add_f32_e32 v96, v211, v96
	v_add_f32_e32 v96, v212, v96
	v_add_f32_e32 v96, v213, v96
	v_add_f32_e32 v96, v214, v96
	v_add_f32_e32 v96, v215, v96
	s_waitcnt lgkmcnt(7)
	v_mfma_f32_32x32x16_f16 v[80:95], v[124:127], v[140:143], v[80:95]
	v_add_f32_e32 v96, v216, v96
	v_add_f32_e32 v96, v217, v96
	v_add_f32_e32 v96, v218, v96
	v_add_f32_e32 v96, v219, v96
	v_add_f32_e32 v96, v220, v96
	v_add_f32_e32 v96, v221, v96
	v_add_f32_e32 v96, v222, v96
	v_exp_f32_e32 v121, v97
	s_waitcnt lgkmcnt(6)
	v_mfma_f32_32x32x16_f16 v[0:15], v[162:165], v[140:143], v[0:15]
	v_add_f32_e32 v96, v223, v96
	v_exp_f32_e32 v122, v98
	v_add_f32_e32 v96, v224, v96
	v_exp_f32_e32 v123, v99
	v_add_f32_e32 v96, v225, v96
	v_add_f32_e32 v96, v120, v96
	v_add_f32_e32 v96, v121, v96
	s_waitcnt lgkmcnt(5)
	v_mfma_f32_32x32x16_f16 v[80:95], v[116:119], v[136:139], v[80:95]
	v_exp_f32_e32 v124, v102
	v_add_f32_e32 v96, v122, v96
	v_exp_f32_e32 v125, v103
	v_add_f32_e32 v96, v123, v96
	v_exp_f32_e32 v126, v104
	v_add_f32_e32 v96, v182, v96
	v_exp_f32_e32 v127, v105
	s_waitcnt lgkmcnt(4)
	v_mfma_f32_32x32x16_f16 v[0:15], v[166:169], v[136:139], v[0:15]
	v_add_f32_e32 v96, v183, v96
	v_add_f32_e32 v96, v124, v96
	v_add_f32_e32 v96, v125, v96
	v_add_f32_e32 v96, v126, v96
	v_exp_f32_e32 v162, v109
	v_add_f32_e32 v96, v127, v96
	v_exp_f32_e32 v163, v110
	s_waitcnt lgkmcnt(3)
	v_mfma_f32_32x32x16_f16 v[80:95], v[112:115], v[132:135], v[80:95]
	v_add_f32_e32 v96, v192, v96
	v_add_f32_e32 v96, v193, v96
	v_add_f32_e32 v96, v194, v96
	v_add_f32_e32 v96, v162, v96
	v_add_f32_e32 v96, v163, v96
	v_add_f32_e32 v96, v111, v96
	v_mov_b32_e32 v97, v96
	s_waitcnt lgkmcnt(2)
	v_mfma_f32_32x32x16_f16 v[0:15], v[170:173], v[132:135], v[0:15]
	v_permlane32_swap_b32_e32 v96, v97
	v_add_f32_e32 v96, v96, v97
	v_add_f32_e32 v185, v185, v96
	v_cvt_pk_f16_f32 v96, v210, v211
	v_cvt_pk_f16_f32 v97, v212, v213
	v_cvt_pk_f16_f32 v98, v214, v215
	s_waitcnt lgkmcnt(1)
	v_mfma_f32_32x32x16_f16 v[80:95], v[174:177], v[128:131], v[80:95]
	v_cvt_pk_f16_f32 v99, v216, v217
	v_cvt_pk_f16_f32 v102, v222, v223
	v_cvt_pk_f16_f32 v103, v224, v225
	v_cvt_pk_f16_f32 v104, v120, v121
	v_cvt_pk_f16_f32 v105, v122, v123
	v_cvt_pk_f16_f32 v107, v124, v125
	v_cvt_pk_f16_f32 v108, v126, v127
	v_cvt_pk_f16_f32 v109, v192, v193
	v_cvt_pk_f16_f32 v110, v194, v162
	v_cvt_pk_f16_f32 v111, v163, v111
	v_permlane32_swap_b32_e32 v96, v98
	v_permlane32_swap_b32_e32 v97, v99
	v_permlane32_swap_b32_e32 v100, v102
	v_permlane32_swap_b32_e32 v101, v103
	v_permlane32_swap_b32_e32 v104, v106
	v_permlane32_swap_b32_e32 v105, v107
	v_permlane32_swap_b32_e32 v108, v110
	v_permlane32_swap_b32_e32 v109, v111
	s_waitcnt lgkmcnt(0)
	v_mfma_f32_32x32x16_f16 v[0:15], v[178:181], v[128:131], v[0:15]
	ds_read_b64_tr_b16 v[112:113], v184 offset:0
	ds_read_b64_tr_b16 v[114:115], v184 offset:0x800
	ds_read_b64_tr_b16 v[116:117], v184 offset:0x1000
	ds_read_b64_tr_b16 v[118:119], v184 offset:0x1800
	ds_read_b64_tr_b16 v[120:121], v184 offset:0x2000
	ds_read_b64_tr_b16 v[122:123], v184 offset:0x2800
	ds_read_b64_tr_b16 v[124:125], v184 offset:0x3000
	ds_read_b64_tr_b16 v[126:127], v184 offset:0x3800
	s_waitcnt lgkmcnt(0)
	s_nop 0
	v_mfma_f32_32x32x16_f16 v[64:79], v[96:99], v[112:115], v[64:79]
	v_exp_f32_e32 v208, v80
	v_exp_f32_e32 v192, v81
	ds_read_b64_tr_b16 v[80:81], v184 offset:0x200
	v_exp_f32_e32 v193, v82
	v_exp_f32_e32 v194, v83
	ds_read_b64_tr_b16 v[82:83], v184 offset:0xa00
	ds_read_b64_tr_b16 v[112:113], v184 offset:0x1200
	v_mfma_f32_32x32x16_f16 v[64:79], v[100:103], v[116:119], v[64:79]
	ds_read_b64_tr_b16 v[114:115], v184 offset:0x1a00
	ds_read_b64_tr_b16 v[116:117], v184 offset:0x2200
	ds_read_b64_tr_b16 v[118:119], v184 offset:0x2a00
	v_mfma_f32_32x32x16_f16 v[64:79], v[104:107], v[120:123], v[64:79]
	ds_read_b64_tr_b16 v[120:121], v184 offset:0x3200
	ds_read_b64_tr_b16 v[122:123], v184 offset:0x3a00
	s_waitcnt lgkmcnt(0)
	v_mfma_f32_32x32x16_f16 v[64:79], v[108:111], v[124:127], v[64:79]
	v_mfma_f32_32x32x16_f16 v[48:63], v[96:99], v[80:83], v[48:63]
	ds_read_b64_tr_b16 v[80:81], v184 offset:0x400
	ds_read_b64_tr_b16 v[82:83], v184 offset:0xc00
	v_exp_f32_e32 v195, v84
	v_exp_f32_e32 v196, v85
	ds_read_b64_tr_b16 v[84:85], v184 offset:0x1400
	v_exp_f32_e32 v197, v86
	v_exp_f32_e32 v198, v87
	v_mfma_f32_32x32x16_f16 v[48:63], v[100:103], v[112:115], v[48:63]
	ds_read_b64_tr_b16 v[86:87], v184 offset:0x1c00
	ds_read_b64_tr_b16 v[112:113], v184 offset:0x2400
	ds_read_b64_tr_b16 v[114:115], v184 offset:0x2c00
	v_mfma_f32_32x32x16_f16 v[48:63], v[104:107], v[116:119], v[48:63]
	ds_read_b64_tr_b16 v[116:117], v184 offset:0x3400
	ds_read_b64_tr_b16 v[118:119], v184 offset:0x3c00
	s_waitcnt lgkmcnt(0)
	v_mfma_f32_32x32x16_f16 v[48:63], v[108:111], v[120:123], v[48:63]
	v_mfma_f32_32x32x16_f16 v[32:47], v[96:99], v[80:83], v[32:47]
	ds_read_b64_tr_b16 v[80:81], v184 offset:0x600
	ds_read_b64_tr_b16 v[82:83], v184 offset:0xe00
	v_exp_f32_e32 v199, v88
	v_exp_f32_e32 v200, v89
	v_exp_f32_e32 v201, v90
	v_exp_f32_e32 v202, v91
	v_mfma_f32_32x32x16_f16 v[32:47], v[100:103], v[84:87], v[32:47]
	ds_read_b64_tr_b16 v[84:85], v184 offset:0x1600
	ds_read_b64_tr_b16 v[86:87], v184 offset:0x1e00
	ds_read_b64_tr_b16 v[88:89], v184 offset:0x2600
	ds_read_b64_tr_b16 v[90:91], v184 offset:0x2e00
	v_mfma_f32_32x32x16_f16 v[32:47], v[104:107], v[112:115], v[32:47]
	ds_read_b64_tr_b16 v[112:113], v184 offset:0x3600
	ds_read_b64_tr_b16 v[114:115], v184 offset:0x3e00
	s_waitcnt lgkmcnt(0)
	v_mfma_f32_32x32x16_f16 v[32:47], v[108:111], v[116:119], v[32:47]
	v_mfma_f32_32x32x16_f16 v[16:31], v[96:99], v[80:83], v[16:31]
	v_exp_f32_e32 v203, v92
	v_exp_f32_e32 v204, v93
	v_exp_f32_e32 v205, v94
	v_exp_f32_e32 v206, v95
	s_waitcnt vmcnt(0) lgkmcnt(0)
	s_barrier
	v_mfma_f32_32x32x16_f16 v[16:31], v[100:103], v[84:87], v[16:31]
	v_mfma_f32_32x32x16_f16 v[16:31], v[104:107], v[88:91], v[16:31]
	v_mfma_f32_32x32x16_f16 v[16:31], v[108:111], v[112:115], v[16:31]
	s_cmp_gt_u32 s100, 8
	s_cbranch_scc1 .Lcw_b_done
	s_cmp_eq_u32 s100, 0
	s_cbranch_scc1 .Lcw_b_load
	v_cvt_pk_f16_f32 v252, v252, v253
	v_cvt_pk_f16_f32 v253, v254, v255
	v_lshrrev_b32_e32 v254, 1, v191
	global_store_dwordx2 v254, v[252:253], s[60:61]
	s_add_u32 s60, s60, 0x1000
	s_addc_u32 s61, s61, 0
	s_cmp_eq_u32 s100, 8
	s_cbranch_scc1 .Lcw_b_inc

.Lcw_b_done:
	s_mov_b32 m0, s91
	s_add_i32 s10, s0, 0xffffa000
	ds_read_b128 v[80:83], v190
	ds_read_b128 v[84:87], v190 offset:8192
	buffer_load_dwordx4 v191, s[68:71], s10 offen lds
	ds_read_b128 v[88:91], v189
	ds_read_b128 v[92:95], v189 offset:8192
	s_add_i32 s10, s0, 0xffffc000
	s_mov_b32 m0, s92
	s_waitcnt lgkmcnt(3)
	v_mfma_f32_32x32x16_f16 v[112:127], v[80:83], v[156:159], -0.5
	s_waitcnt lgkmcnt(2)
	v_mfma_f32_32x32x16_f16 v[96:111], v[84:87], v[156:159], -0.5
	buffer_load_dwordx4 v191, s[68:71], s10 offen lds
	ds_read_b128 v[80:83], v188
	ds_read_b128 v[84:87], v188 offset:8192
	s_waitcnt lgkmcnt(3)
	v_mfma_f32_32x32x16_f16 v[112:127], v[88:91], v[152:155], v[112:127]
	s_add_i32 s10, s0, 0xffffe000
	s_mov_b32 m0, s93
	s_nop 0
	buffer_load_dwordx4 v191, s[68:71], s10 offen lds
	s_mov_b32 m0, s94
	s_waitcnt lgkmcnt(1)
	v_mfma_f32_32x32x16_f16 v[112:127], v[80:83], v[148:151], v[112:127]
	ds_read_b128 v[80:83], v187
	ds_read_b128 v[88:91], v187 offset:8192
	buffer_load_dwordx4 v191, s[68:71], s0 offen lds
	s_mov_b32 m0, s3
	v_mfma_f32_32x32x16_f16 v[96:111], v[92:95], v[152:155], v[96:111]
	ds_read_b128 v[92:95], v190 offset:128
	ds_read_b128 v[162:165], v190 offset:8320
	buffer_load_dwordx4 v186, s[72:75], s5 offen lds
	s_mov_b32 m0, s82
	ds_read_b128 v[166:169], v189 offset:128
	ds_read_b128 v[170:173], v189 offset:8320
	buffer_load_dwordx4 v186, s[72:75], s6 offen lds
	s_mov_b32 m0, s81
	ds_read_b128 v[174:177], v188 offset:128
	ds_read_b128 v[178:181], v188 offset:8320
	buffer_load_dwordx4 v186, s[72:75], s7 offen lds
	s_mov_b32 m0, s80
	ds_read_b128 v[210:213], v187 offset:128
	ds_read_b128 v[214:217], v187 offset:8320
	buffer_load_dwordx4 v186, s[72:75], s9 offen lds
	s_waitcnt lgkmcnt(10)
	v_mfma_f32_32x32x16_f16 v[96:111], v[84:87], v[148:151], v[96:111]
	v_exp_f32_e32 v84, v4
	v_exp_f32_e32 v85, v5
	v_exp_f32_e32 v86, v6
	v_exp_f32_e32 v87, v7
	v_cvt_pk_f16_f32 v4, v199, v200
	v_cvt_pk_f16_f32 v5, v201, v202
	v_cvt_pk_f16_f32 v6, v203, v204
	s_waitcnt lgkmcnt(8)
	v_mfma_f32_32x32x16_f16 v[96:111], v[88:91], v[144:147], v[96:111]
	v_exp_f32_e32 v88, v8
	v_exp_f32_e32 v89, v9
	v_exp_f32_e32 v90, v10
	v_exp_f32_e32 v91, v11
	v_cvt_pk_f16_f32 v7, v205, v206
	v_cvt_pk_f16_f32 v10, v84, v85
	v_cvt_pk_f16_f32 v11, v86, v87
	v_mfma_f32_32x32x16_f16 v[112:127], v[80:83], v[144:147], v[112:127]
	v_exp_f32_e32 v80, v0
	v_add_f32_e32 v0, 0, v208
	v_add_f32_e32 v0, v192, v0
	v_add_f32_e32 v0, v193, v0
	v_add_f32_e32 v0, v194, v0
	v_add_f32_e32 v0, v195, v0
	v_add_f32_e32 v0, v196, v0
	s_waitcnt lgkmcnt(6)
	v_mfma_f32_32x32x16_f16 v[96:111], v[162:165], v[140:143], v[96:111]
	v_add_f32_e32 v0, v197, v0
	v_add_f32_e32 v0, v198, v0
	v_add_f32_e32 v0, v199, v0
	v_add_f32_e32 v0, v200, v0
	v_add_f32_e32 v0, v201, v0
	v_add_f32_e32 v0, v202, v0
	v_add_f32_e32 v0, v203, v0
	v_mfma_f32_32x32x16_f16 v[112:127], v[92:95], v[140:143], v[112:127]
	v_exp_f32_e32 v81, v1
	v_add_f32_e32 v0, v204, v0
	v_exp_f32_e32 v82, v2
	v_add_f32_e32 v0, v205, v0
	v_exp_f32_e32 v83, v3
	v_add_f32_e32 v0, v206, v0
	v_add_f32_e32 v0, v80, v0
	s_waitcnt lgkmcnt(4)
	v_mfma_f32_32x32x16_f16 v[96:111], v[170:173], v[136:139], v[96:111]
	v_add_f32_e32 v0, v81, v0
	v_add_f32_e32 v0, v82, v0
	v_add_f32_e32 v0, v83, v0
	v_add_f32_e32 v0, v84, v0
	v_add_f32_e32 v0, v85, v0
	v_add_f32_e32 v0, v86, v0
	v_add_f32_e32 v0, v87, v0
	v_mfma_f32_32x32x16_f16 v[112:127], v[166:169], v[136:139], v[112:127]
	v_exp_f32_e32 v92, v12
	v_add_f32_e32 v0, v88, v0
	v_exp_f32_e32 v93, v13
	v_add_f32_e32 v0, v89, v0
	v_exp_f32_e32 v94, v14
	v_add_f32_e32 v0, v90, v0
	v_exp_f32_e32 v95, v15
	s_waitcnt lgkmcnt(2)
	v_mfma_f32_32x32x16_f16 v[96:111], v[178:181], v[132:135], v[96:111]
	v_add_f32_e32 v0, v91, v0
	v_add_f32_e32 v0, v92, v0
	v_add_f32_e32 v0, v93, v0
	v_add_f32_e32 v0, v94, v0
	v_add_f32_e32 v0, v95, v0
	v_mov_b32_e32 v1, v0
	s_nop 1
	v_permlane32_swap_b32_e32 v0, v1
	v_mfma_f32_32x32x16_f16 v[112:127], v[174:177], v[132:135], v[112:127]
	v_add_f32_e32 v0, v0, v1
	v_add_f32_e32 v185, v185, v0
	v_cvt_pk_f16_f32 v0, v208, v192
	v_cvt_pk_f16_f32 v1, v193, v194
	v_cvt_pk_f16_f32 v2, v195, v196
	v_cvt_pk_f16_f32 v3, v197, v198
	v_cvt_pk_f16_f32 v8, v80, v81
	s_waitcnt lgkmcnt(0)
	v_mfma_f32_32x32x16_f16 v[96:111], v[214:217], v[128:131], v[96:111]
	v_cvt_pk_f16_f32 v9, v82, v83
	v_cvt_pk_f16_f32 v12, v88, v89
	v_cvt_pk_f16_f32 v13, v90, v91
	v_cvt_pk_f16_f32 v14, v92, v93
	v_cvt_pk_f16_f32 v15, v94, v95
	v_permlane32_swap_b32_e32 v0, v2
	v_mfma_f32_32x32x16_f16 v[112:127], v[210:213], v[128:131], v[112:127]
	v_permlane32_swap_b32_e32 v1, v3
	v_permlane32_swap_b32_e32 v4, v6
	v_permlane32_swap_b32_e32 v5, v7
	v_permlane32_swap_b32_e32 v8, v10
	v_permlane32_swap_b32_e32 v9, v11
	v_permlane32_swap_b32_e32 v12, v14
	v_permlane32_swap_b32_e32 v13, v15
	ds_read_b64_tr_b16 v[162:163], v184 offset:0x8000
	ds_read_b64_tr_b16 v[164:165], v184 offset:0x8800
	ds_read_b64_tr_b16 v[166:167], v184 offset:0x9000
	ds_read_b64_tr_b16 v[168:169], v184 offset:0x9800
	ds_read_b64_tr_b16 v[170:171], v184 offset:0xa000
	ds_read_b64_tr_b16 v[172:173], v184 offset:0xa800
	ds_read_b64_tr_b16 v[174:175], v184 offset:0xb000
	ds_read_b64_tr_b16 v[176:177], v184 offset:0xb800
	s_waitcnt lgkmcnt(0)
	s_nop 0
	v_mfma_f32_32x32x16_f16 v[64:79], v[0:3], v[162:165], v[64:79]
	s_nop 2
	v_exp_f32_e32 v210, v112
	v_exp_f32_e32 v211, v113
	ds_read_b64_tr_b16 v[112:113], v184 offset:0x8200
	v_exp_f32_e32 v212, v114
	v_exp_f32_e32 v213, v115
	ds_read_b64_tr_b16 v[114:115], v184 offset:0x8a00
	ds_read_b64_tr_b16 v[162:163], v184 offset:0x9200
	v_mfma_f32_32x32x16_f16 v[64:79], v[4:7], v[166:169], v[64:79]
	ds_read_b64_tr_b16 v[164:165], v184 offset:0x9a00
	ds_read_b64_tr_b16 v[166:167], v184 offset:0xa200
	ds_read_b64_tr_b16 v[168:169], v184 offset:0xaa00
	v_mfma_f32_32x32x16_f16 v[64:79], v[8:11], v[170:173], v[64:79]
	ds_read_b64_tr_b16 v[170:171], v184 offset:0xb200
	ds_read_b64_tr_b16 v[172:173], v184 offset:0xba00
	s_waitcnt lgkmcnt(0)
	v_mfma_f32_32x32x16_f16 v[64:79], v[12:15], v[174:177], v[64:79]
	v_mfma_f32_32x32x16_f16 v[48:63], v[0:3], v[112:115], v[48:63]
	ds_read_b64_tr_b16 v[112:113], v184 offset:0x8400
	ds_read_b64_tr_b16 v[114:115], v184 offset:0x8c00
	v_exp_f32_e32 v214, v116
	v_exp_f32_e32 v215, v117
	ds_read_b64_tr_b16 v[116:117], v184 offset:0x9400
	v_exp_f32_e32 v216, v118
	v_exp_f32_e32 v217, v119
	v_mfma_f32_32x32x16_f16 v[48:63], v[4:7], v[162:165], v[48:63]
	ds_read_b64_tr_b16 v[118:119], v184 offset:0x9c00
	ds_read_b64_tr_b16 v[162:163], v184 offset:0xa400
	ds_read_b64_tr_b16 v[164:165], v184 offset:0xac00
	v_mfma_f32_32x32x16_f16 v[48:63], v[8:11], v[166:169], v[48:63]
	ds_read_b64_tr_b16 v[166:167], v184 offset:0xb400
	ds_read_b64_tr_b16 v[168:169], v184 offset:0xbc00
	s_waitcnt lgkmcnt(0)
	v_mfma_f32_32x32x16_f16 v[48:63], v[12:15], v[170:173], v[48:63]
	v_mfma_f32_32x32x16_f16 v[32:47], v[0:3], v[112:115], v[32:47]
	ds_read_b64_tr_b16 v[112:113], v184 offset:0x8600
	ds_read_b64_tr_b16 v[114:115], v184 offset:0x8e00
	v_exp_f32_e32 v218, v120
	v_exp_f32_e32 v219, v121
	v_exp_f32_e32 v220, v122
	v_exp_f32_e32 v221, v123
	v_mfma_f32_32x32x16_f16 v[32:47], v[4:7], v[116:119], v[32:47]
	ds_read_b64_tr_b16 v[116:117], v184 offset:0x9600
	ds_read_b64_tr_b16 v[118:119], v184 offset:0x9e00
	ds_read_b64_tr_b16 v[120:121], v184 offset:0xa600
	ds_read_b64_tr_b16 v[122:123], v184 offset:0xae00
	v_mfma_f32_32x32x16_f16 v[32:47], v[8:11], v[162:165], v[32:47]
	ds_read_b64_tr_b16 v[162:163], v184 offset:0xb600
	ds_read_b64_tr_b16 v[164:165], v184 offset:0xbe00
	s_waitcnt lgkmcnt(0)
	v_mfma_f32_32x32x16_f16 v[32:47], v[12:15], v[166:169], v[32:47]
	v_mfma_f32_32x32x16_f16 v[16:31], v[0:3], v[112:115], v[16:31]
	v_exp_f32_e32 v222, v124
	v_exp_f32_e32 v223, v125
	v_exp_f32_e32 v224, v126
	v_exp_f32_e32 v225, v127
	s_waitcnt vmcnt(0) lgkmcnt(0)
	s_barrier
	v_mfma_f32_32x32x16_f16 v[16:31], v[4:7], v[116:119], v[16:31]
	v_mfma_f32_32x32x16_f16 v[16:31], v[8:11], v[120:123], v[16:31]
	v_mfma_f32_32x32x16_f16 v[16:31], v[12:15], v[162:165], v[16:31]
	s_add_i32 s97, s97, 2
	s_add_i32 s1, s1, 4
	s_add_i32 s0, s0, 0x10000
	s_cmp_le_u32 s1, s99
	s_cbranch_scc1 .LBB3_3
	v_mul_i32_i24_e32 v0, -4, v160
	s_lshl_b32 s0, s4, 6
	v_subrev_u32_e32 v209, s0, v0
	s_cmp_gt_u32 s97, s99
	v_add_u32_e32 v160, v209, v161
	s_cbranch_scc1 .LBB3_18
	s_cmp_lt_u32 s97, s99
	s_cselect_b64 s[6:7], -1, 0
	s_cmp_ge_u32 s97, s99
	s_cselect_b64 s[4:5], -1, 0
	ds_read_b128 v[80:83], v190 offset:32768
	ds_read_b128 v[112:115], v190 offset:40960
	s_and_b64 vcc, exec, s[4:5]
	s_waitcnt lgkmcnt(1)
	v_mfma_f32_32x32x16_f16 v[0:15], v[80:83], v[156:159], -0.5
	s_waitcnt lgkmcnt(0)
	v_mfma_f32_32x32x16_f16 v[80:95], v[112:115], v[156:159], -0.5
	s_cbranch_vccnz .LBB3_7
	s_lshl_b32 s0, s97, 15
	s_add_i32 s0, s0, 0x8000
	s_mov_b32 m0, s86
	s_nop 0
	buffer_load_dwordx4 v191, s[68:71], s0 offen lds

	.amdhsa_kernel _Z12attn_splitkvPKDF16_S0_S0_PDF16_
		.amdhsa_group_segment_fixed_size 0
		.amdhsa_private_segment_fixed_size 0
		.amdhsa_kernarg_size 32
		.amdhsa_user_sgpr_count 2
		.amdhsa_user_sgpr_dispatch_ptr 0
		.amdhsa_user_sgpr_queue_ptr 0
		.amdhsa_user_sgpr_kernarg_segment_ptr 1
		.amdhsa_user_sgpr_dispatch_id 0
		.amdhsa_user_sgpr_kernarg_preload_length 0
		.amdhsa_user_sgpr_kernarg_preload_offset 0
		.amdhsa_user_sgpr_private_segment_size 0
		.amdhsa_uses_dynamic_stack 0
		.amdhsa_enable_private_segment 0
		.amdhsa_system_sgpr_workgroup_id_x 1
		.amdhsa_system_sgpr_workgroup_id_y 0
		.amdhsa_system_sgpr_workgroup_id_z 0
		.amdhsa_system_sgpr_workgroup_info 0
		.amdhsa_system_vgpr_workitem_id 0
		.amdhsa_next_free_vgpr 256
		.amdhsa_next_free_sgpr 102
		.amdhsa_accum_offset 256
		.amdhsa_reserve_vcc 1
		.amdhsa_float_round_mode_32 0
		.amdhsa_float_round_mode_16_64 0
		.amdhsa_float_denorm_mode_32 3
		.amdhsa_float_denorm_mode_16_64 3
		.amdhsa_dx10_clamp 1
		.amdhsa_ieee_mode 1
		.amdhsa_fp16_overflow 0
		.amdhsa_tg_split 0
		.amdhsa_exception_fp_ieee_invalid_op 0
		.amdhsa_exception_fp_denorm_src 0
		.amdhsa_exception_fp_ieee_div_zero 0
		.amdhsa_exception_fp_ieee_overflow 0
		.amdhsa_exception_fp_ieee_underflow 0
		.amdhsa_exception_fp_ieee_inexact 0
		.amdhsa_exception_int_div_zero 0
	.end_amdhsa_kernel

amdhsa.kernels:
  - .agpr_count:     0
    .args:
      - .actual_access:  read_only
        .address_space:  global
        .offset:         0
        .size:           8
        .value_kind:     global_buffer
      - .actual_access:  write_only
        .address_space:  global
        .offset:         8
        .size:           8
        .value_kind:     global_buffer
      - .offset:         16
        .size:           4
        .value_kind:     by_value
      - .actual_access:  read_only
        .address_space:  global
        .offset:         24
        .size:           8
        .value_kind:     global_buffer
      - .actual_access:  write_only
        .address_space:  global
        .offset:         32
        .size:           8
        .value_kind:     global_buffer
      - .offset:         40
        .size:           4
        .value_kind:     by_value
      - .actual_access:  read_only
        .address_space:  global
        .offset:         48
        .size:           8
        .value_kind:     global_buffer
      - .actual_access:  write_only
        .address_space:  global
        .offset:         56
        .size:           8
        .value_kind:     global_buffer
      - .offset:         64
        .size:           4
        .value_kind:     by_value
      - .actual_access:  write_only
        .address_space:  global
        .offset:         72
        .size:           8
        .value_kind:     global_buffer
      - .actual_access:  write_only
        .address_space:  global
        .offset:         80
        .size:           8
        .value_kind:     global_buffer
    .group_segment_fixed_size: 0
    .kernarg_segment_align: 8
    .kernarg_segment_size: 88
    .language:       OpenCL C
    .language_version:
      - 2
      - 0
    .max_flat_workgroup_size: 256
    .name:           _Z8cvt3_f16PKfPDF16_iS0_S1_iS0_S1_iPfS2_
    .private_segment_fixed_size: 0
    .sgpr_count:     18
    .sgpr_spill_count: 0
    .symbol:         _Z8cvt3_f16PKfPDF16_iS0_S1_iS0_S1_iPfS2_.kd
    .uniform_work_group_size: 1
    .uses_dynamic_stack: false
    .vgpr_count:     24
    .vgpr_spill_count: 0
    .wavefront_size: 64
  - .agpr_count:     0
    .args:
      - .actual_access:  read_only
        .address_space:  global
        .offset:         0
        .size:           8
        .value_kind:     global_buffer
      - .actual_access:  read_only
        .address_space:  global
        .offset:         8
        .size:           8
        .value_kind:     global_buffer
      - .actual_access:  write_only
        .address_space:  global
        .offset:         16
        .size:           8
        .value_kind:     global_buffer
      - .offset:         24
        .size:           56
        .value_kind:     by_value
    .group_segment_fixed_size: 0
    .kernarg_segment_align: 8
    .kernarg_segment_size: 80
    .language:       OpenCL C
    .language_version:
      - 2
      - 0
    .max_flat_workgroup_size: 512
    .name:           _Z10gemm_cprojPKDF16_S0_Pf7EpiArgs
    .private_segment_fixed_size: 0
    .sgpr_count:     44
    .sgpr_spill_count: 0
    .symbol:         _Z10gemm_cprojPKDF16_S0_Pf7EpiArgs.kd
    .uniform_work_group_size: 1
    .uses_dynamic_stack: false
    .vgpr_count:     140
    .vgpr_spill_count: 0
    .wavefront_size: 64
  - .agpr_count:     0
    .args:
      - .actual_access:  read_only
        .address_space:  global
        .offset:         0
        .size:           8
        .value_kind:     global_buffer
      - .actual_access:  read_only
        .address_space:  global
        .offset:         8
        .size:           8
        .value_kind:     global_buffer
      - .offset:         16
        .size:           56
        .value_kind:     by_value
    .group_segment_fixed_size: 0
    .kernarg_segment_align: 8
    .kernarg_segment_size: 72
    .language:       OpenCL C
    .language_version:
      - 2
      - 0
    .max_flat_workgroup_size: 512
    .name:           _Z8gemm_qkvPKDF16_S0_7EpiArgs
    .private_segment_fixed_size: 0
    .sgpr_count:     55
    .sgpr_spill_count: 0
    .symbol:         _Z8gemm_qkvPKDF16_S0_7EpiArgs.kd
    .uniform_work_group_size: 1
    .uses_dynamic_stack: false
    .vgpr_count:     236
    .vgpr_spill_count: 0
    .wavefront_size: 64
  - .agpr_count:     0
    .args:
      - .actual_access:  read_only
        .address_space:  global
        .offset:         0
        .size:           8
        .value_kind:     global_buffer
      - .actual_access:  read_only
        .address_space:  global
        .offset:         8
        .size:           8
        .value_kind:     global_buffer
      - .actual_access:  read_only
        .address_space:  global
        .offset:         16
        .size:           8
        .value_kind:     global_buffer
      - .actual_access:  write_only
        .address_space:  global
        .offset:         24
        .size:           8
        .value_kind:     global_buffer
    .group_segment_fixed_size: 0
    .kernarg_segment_align: 8
    .kernarg_segment_size: 32
    .language:       OpenCL C
    .language_version:
      - 2
      - 0
    .max_flat_workgroup_size: 512
    .name:           _Z12attn_splitkvPKDF16_S0_S0_PDF16_
    .private_segment_fixed_size: 0
    .sgpr_count:     108
    .sgpr_spill_count: 1
    .symbol:         _Z12attn_splitkvPKDF16_S0_S0_PDF16_.kd
    .uniform_work_group_size: 1
    .uses_dynamic_stack: false
    .vgpr_count:     256
    .vgpr_spill_count: 0
    .wavefront_size: 64
